# adds the same LDS read pipelining to the MLA attention tile loop (K fragment reads 6 deep under counted waits, V group prefetch) on top of the P13 change
# speedup vs baseline: 1.0175x; 1.0125x over previous
; #define PSUB_AT(k) do { if (PROBE_SUB == (k) && DK == PROBE_SUBDK) sacc = __builtin_amdgcn_readfirstlane(sacc + ((unsigned)__builtin_readcyclecounter() - ps_t0_)); } while (0)
; #define SBAR() __builtin_amdgcn_sched_barrier(0)
; #define SLOAD(k0) do { const unsigned so_k = (unsigned)((k0) * ldk) * 2u, so_v = (unsigned)((k0) * ldv) * 2u; \
;         _Pragma("unroll") for (int i = 0; i < KP; ++i) ks[i] = __builtin_amdgcn_raw_buffer_load_b128(krs, kgo[i], so_k, 0); \
;         vs0 = __builtin_amdgcn_raw_buffer_load_b128(vrs, vgo, so_v, 0); vs1 = __builtin_amdgcn_raw_buffer_load_b128(vrs, vgo + vstep, so_v, 0); } while (0)
; template <int DK, bool PF, bool EARLY, bool PFD = false> ...
;     ...
;         const char* Kb = K_lds + cur * SHM_K;
; #pragma unroll
;         for (int d0 = 0; d0 < NQ; ++d0) {
;             const bf16x8 b0 = *reinterpret_cast<const bf16x8*>(Kb + kra_(d0 & 3) + (d0 >> 2) * 128);
;             const bf16x8 b1 = *reinterpret_cast<const bf16x8*>(Kb + kra_(d0 & 3) + (d0 >> 2) * 128 + 32 * DK * 2);
;             p0 = __builtin_amdgcn_mfma_f32_32x32x16_bf16(b0, qr[d0], p0, 0, 0, 0);
;             p1 = __builtin_amdgcn_mfma_f32_32x32x16_bf16(b1, qr[d0], p1, 0, 0, 0);
;             if ((d0 & 3) == 3) SBAR();
;         }
;         PSUB_AT(1);
;         if (!EARLY && j + 1 < ntile) SLOAD((j + 1) * 64);
;         float ps = 0.f, ps1 = 0.f;
; #pragma unroll
;         for (int r = 0; r < 16; ++r) { p0[r] = __builtin_amdgcn_exp2f(p0[r]); p1[r] = __builtin_amdgcn_exp2f(p1[r]); ps += p0[r]; asm("" : "+v"(ps)); ps1 += p1[r]; asm("" : "+v"(ps1)); }
;         l_reg += ps + ps1;
;         bf16x8 pa0, pa1, pa2, pa3;
;     ...
;         PK4(p0, 0, pa0); PK4(p0, 8, pa1); PK4(p1, 0, pa2); PK4(p1, 8, pa3);
;     ...
;         PSUB_AT(2);
;         const int vb = vb0 + cur * SHM_V;
;         pv_one<0>(o[0], vb, pa0, pa1, pa2, pa3); pv_one<1>(o[1], vb, pa0, pa1, pa2, pa3); pv_one<2>(o[2], vb, pa0, pa1, pa2, pa3); pv_one<3>(o[3], vb, pa0, pa1, pa2, pa3);
.LBB0_1200:
	s_and_b32 s23, s19, 1
	s_mul_i32 s24, s23, 0x6000
	v_add_u32_e32 v250, s24, v207
	v_add_u32_e32 v251, v250, v201
	v_add_u32_e32 v252, v250, v214
	v_add_u32_e32 v253, v250, v215
	v_add_u32_e32 v245, v250, v216
	ds_read_b128 v[162:165], v251 offset:32768
	ds_read_b128 v[166:169], v251 offset:45056
	ds_read_b128 v[170:173], v252 offset:32768
	ds_read_b128 v[174:177], v252 offset:45056
	ds_read_b128 v[178:181], v253 offset:32768
	ds_read_b128 v[246:249], v253 offset:45056
	s_waitcnt lgkmcnt(5)
	v_mfma_f32_32x32x16_bf16 v[98:113], v[162:165], v[158:161], v[66:81]
	ds_read_b128 v[162:165], v245 offset:32768
	s_waitcnt lgkmcnt(5)
	v_mfma_f32_32x32x16_bf16 v[82:97], v[166:169], v[158:161], v[66:81]
	ds_read_b128 v[166:169], v245 offset:45056
	s_waitcnt lgkmcnt(5)
	v_mfma_f32_32x32x16_bf16 v[98:113], v[170:173], v[154:157], v[98:113]
	ds_read_b128 v[170:173], v251 offset:32896
	s_waitcnt lgkmcnt(5)
	v_mfma_f32_32x32x16_bf16 v[82:97], v[174:177], v[154:157], v[82:97]
	ds_read_b128 v[174:177], v251 offset:45184
	s_waitcnt lgkmcnt(5)
	v_mfma_f32_32x32x16_bf16 v[98:113], v[178:181], v[150:153], v[98:113]
	ds_read_b128 v[178:181], v252 offset:32896
	s_waitcnt lgkmcnt(5)
	v_mfma_f32_32x32x16_bf16 v[82:97], v[246:249], v[150:153], v[82:97]
	ds_read_b128 v[246:249], v252 offset:45184
	s_waitcnt lgkmcnt(5)
	v_mfma_f32_32x32x16_bf16 v[98:113], v[162:165], v[146:149], v[98:113]
	ds_read_b128 v[162:165], v253 offset:32896
	s_waitcnt lgkmcnt(5)
	v_mfma_f32_32x32x16_bf16 v[82:97], v[166:169], v[146:149], v[82:97]
	ds_read_b128 v[166:169], v253 offset:45184
	s_waitcnt lgkmcnt(5)
	v_mfma_f32_32x32x16_bf16 v[98:113], v[170:173], v[142:145], v[98:113]
	ds_read_b128 v[170:173], v245 offset:32896
	s_waitcnt lgkmcnt(5)
	v_mfma_f32_32x32x16_bf16 v[82:97], v[174:177], v[142:145], v[82:97]
	ds_read_b128 v[174:177], v245 offset:45184
	s_waitcnt lgkmcnt(5)
	v_mfma_f32_32x32x16_bf16 v[98:113], v[178:181], v[138:141], v[98:113]
	ds_read_b128 v[178:181], v251 offset:33024
	s_waitcnt lgkmcnt(5)
	v_mfma_f32_32x32x16_bf16 v[82:97], v[246:249], v[138:141], v[82:97]
	ds_read_b128 v[246:249], v251 offset:45312
	s_waitcnt lgkmcnt(5)
	v_mfma_f32_32x32x16_bf16 v[98:113], v[162:165], v[134:137], v[98:113]
	ds_read_b128 v[162:165], v252 offset:33024
	s_waitcnt lgkmcnt(5)
	v_mfma_f32_32x32x16_bf16 v[82:97], v[166:169], v[134:137], v[82:97]
	ds_read_b128 v[166:169], v252 offset:45312
	s_waitcnt lgkmcnt(5)
	v_mfma_f32_32x32x16_bf16 v[98:113], v[170:173], v[130:133], v[98:113]
	ds_read_b128 v[170:173], v253 offset:33024
	s_waitcnt lgkmcnt(5)
	v_mfma_f32_32x32x16_bf16 v[82:97], v[174:177], v[130:133], v[82:97]
	ds_read_b128 v[174:177], v253 offset:45312
	s_waitcnt lgkmcnt(5)
	v_mfma_f32_32x32x16_bf16 v[98:113], v[178:181], v[126:129], v[98:113]
	ds_read_b128 v[178:181], v245 offset:33024
	s_waitcnt lgkmcnt(5)
	v_mfma_f32_32x32x16_bf16 v[82:97], v[246:249], v[126:129], v[82:97]
	ds_read_b128 v[246:249], v245 offset:45312
	s_waitcnt lgkmcnt(5)
	v_mfma_f32_32x32x16_bf16 v[98:113], v[162:165], v[122:125], v[98:113]
	s_waitcnt lgkmcnt(4)
	v_mfma_f32_32x32x16_bf16 v[82:97], v[166:169], v[122:125], v[82:97]
	s_waitcnt lgkmcnt(3)
	v_mfma_f32_32x32x16_bf16 v[98:113], v[170:173], v[118:121], v[98:113]
	s_waitcnt lgkmcnt(2)
	v_mfma_f32_32x32x16_bf16 v[82:97], v[174:177], v[118:121], v[82:97]
	s_waitcnt lgkmcnt(1)
	v_mfma_f32_32x32x16_bf16 v[98:113], v[178:181], v[114:117], v[98:113]
	s_waitcnt lgkmcnt(0)
	v_mfma_f32_32x32x16_bf16 v[82:97], v[246:249], v[114:117], v[82:97]
	buffer_load_dwordx4 v[166:169], v185, s[8:11], s20 offen
	buffer_load_dwordx4 v[162:165], v191, s[8:11], s20 offen
	buffer_load_dwordx4 v[178:181], v195, s[8:11], s20 offen
	buffer_load_dwordx4 v[170:173], v199, s[12:15], s21 offen
	buffer_load_dwordx4 v[174:177], v203, s[12:15], s21 offen
	s_lshl_b32 s33, s23, 14
	v_add_u32_e32 v245, s33, v209
	ds_read_b64_tr_b16 v[246:247], v245 offset:0x0
	ds_read_b64_tr_b16 v[248:249], v245 offset:0x800
	ds_read_b64_tr_b16 v[250:251], v245 offset:0x1000
	ds_read_b64_tr_b16 v[252:253], v245 offset:0x1800
	s_nop 6
	v_exp_f32_e32 v240, v82
	v_exp_f32_e32 v98, v98
	v_exp_f32_e32 v242, v83
	v_exp_f32_e32 v99, v99
	v_add_f32_e32 v241, 0, v240
	v_add_f32_e32 v82, 0, v98
	v_exp_f32_e32 v83, v100
	v_add_f32_e32 v100, v242, v241
	v_exp_f32_e32 v241, v84
	v_add_f32_e32 v82, v99, v82
	v_exp_f32_e32 v84, v101
	v_exp_f32_e32 v101, v85
	v_add_f32_e32 v82, v83, v82
	v_exp_f32_e32 v85, v102
	v_add_f32_e32 v100, v241, v100
	v_exp_f32_e32 v102, v86
	v_add_f32_e32 v82, v84, v82
	v_exp_f32_e32 v86, v103
	v_add_f32_e32 v100, v101, v100
	v_exp_f32_e32 v103, v87
	v_add_f32_e32 v82, v85, v82
	v_exp_f32_e32 v87, v104
	v_add_f32_e32 v100, v102, v100
	v_exp_f32_e32 v104, v88
	v_add_f32_e32 v82, v86, v82
	v_exp_f32_e32 v88, v105
	v_add_f32_e32 v100, v103, v100
	v_exp_f32_e32 v105, v89
	v_add_f32_e32 v82, v87, v82
	v_exp_f32_e32 v89, v106
	v_add_f32_e32 v100, v104, v100
	v_exp_f32_e32 v106, v90
	v_add_f32_e32 v82, v88, v82
	v_exp_f32_e32 v90, v107
	v_add_f32_e32 v100, v105, v100
	v_exp_f32_e32 v107, v91
	v_add_f32_e32 v82, v89, v82
	v_exp_f32_e32 v91, v108
	v_add_f32_e32 v100, v106, v100
	v_exp_f32_e32 v108, v92
	v_add_f32_e32 v82, v90, v82
	v_exp_f32_e32 v92, v109
	v_add_f32_e32 v100, v107, v100
	v_exp_f32_e32 v109, v93
	v_add_f32_e32 v82, v91, v82
	v_exp_f32_e32 v93, v110
	v_add_f32_e32 v100, v108, v100
	v_exp_f32_e32 v110, v94
	v_add_f32_e32 v82, v92, v82
	v_exp_f32_e32 v94, v111
	v_add_f32_e32 v100, v109, v100
	v_exp_f32_e32 v111, v95
	v_add_f32_e32 v82, v93, v82
	v_exp_f32_e32 v95, v112
	v_add_f32_e32 v100, v110, v100
	v_exp_f32_e32 v112, v96
	v_add_f32_e32 v82, v94, v82
	v_exp_f32_e32 v96, v113
	v_add_f32_e32 v100, v111, v100
	v_exp_f32_e32 v97, v97
	v_add_f32_e32 v82, v95, v82
	v_add_f32_e32 v100, v112, v100
	v_add_f32_e32 v82, v96, v82
	v_add_f32_e32 v100, v97, v100
	s_lshl_b32 s24, s23, 14
	v_add_f32_e32 v82, v82, v100
	v_add_f32_e32 v188, v188, v82
	v_cvt_pk_bf16_f32 v82, v98, v99
	v_cvt_pk_bf16_f32 v83, v83, v84
	v_cvt_pk_bf16_f32 v84, v85, v86
	v_cvt_pk_bf16_f32 v85, v87, v88
	v_cvt_pk_bf16_f32 v86, v89, v90
	v_cvt_pk_bf16_f32 v87, v91, v92
	v_cvt_pk_bf16_f32 v88, v93, v94
	v_cvt_pk_bf16_f32 v89, v95, v96
	v_cvt_pk_bf16_f32 v90, v240, v242
	v_cvt_pk_bf16_f32 v91, v241, v101
	v_cvt_pk_bf16_f32 v92, v102, v103
	v_cvt_pk_bf16_f32 v93, v104, v105
	v_cvt_pk_bf16_f32 v94, v106, v107
	v_cvt_pk_bf16_f32 v95, v108, v109
	v_cvt_pk_bf16_f32 v96, v110, v111
	v_cvt_pk_bf16_f32 v97, v112, v97
	v_add_u32_e32 v244, s24, v209
	ds_read_b64_tr_b16 v[106:107], v244 offset:0x2000
	ds_read_b64_tr_b16 v[108:109], v244 offset:0x2800
	ds_read_b64_tr_b16 v[110:111], v244 offset:0x3000
	ds_read_b64_tr_b16 v[112:113], v244 offset:0x3800
	s_add_i32 s19, s19, 1
	v_permlane32_swap_b32_e32 v82, v84
	v_permlane32_swap_b32_e32 v83, v85
	v_permlane32_swap_b32_e32 v86, v88
	v_permlane32_swap_b32_e32 v87, v89
	v_permlane32_swap_b32_e32 v90, v92
	v_permlane32_swap_b32_e32 v91, v93
	v_permlane32_swap_b32_e32 v94, v96
	v_permlane32_swap_b32_e32 v95, v97
	s_waitcnt lgkmcnt(4)
; #define PSUB_AT(k) do { if (PROBE_SUB == (k) && DK == PROBE_SUBDK) sacc = __builtin_amdgcn_readfirstlane(sacc + ((unsigned)__builtin_readcyclecounter() - ps_t0_)); } while (0)
; #define SBAR() __builtin_amdgcn_sched_barrier(0)
; template <int OFF> __device__ __forceinline__ s16x4 tr_read(int vb) { s16x4 r; asm volatile("ds_read_b64_tr_b16 %0, %1 offset:%2" : "=&v"(r) : "v"(vb), "i"(OFF) : "memory"); return r; }
; #define SWRITE(b) do { _Pragma("unroll") for (int i = 0; i < KP; ++i) *reinterpret_cast<u32x4*>(K_lds + (b) * SHM_K + kst[i]) = ks[i]; \
;         *reinterpret_cast<u32x4*>(V_lds + (b) * SHM_V + vst0) = vs0; *reinterpret_cast<u32x4*>(V_lds + (b) * SHM_V + vst0 + vst1d) = vs1; } while (0)
; template <int D0> __device__ __forceinline__ void pv_one(f32x16& od, int vb, bf16x8 pa0, bf16x8 pa1, bf16x8 pa2, bf16x8 pa3) {
;     const s16x4 l0 = tr_read<v_rd_off(D0, 0, 0)>(vb), h0 = tr_read<v_rd_off(D0, 0, 1)>(vb), l1 = tr_read<v_rd_off(D0, 1, 0)>(vb), h1 = tr_read<v_rd_off(D0, 1, 1)>(vb);
;     const s16x4 l2 = tr_read<v_rd_off(D0, 2, 0)>(vb), h2 = tr_read<v_rd_off(D0, 2, 1)>(vb), l3 = tr_read<v_rd_off(D0, 3, 0)>(vb), h3 = tr_read<v_rd_off(D0, 3, 1)>(vb);
;     asm volatile("s_waitcnt lgkmcnt(0)" ::: "memory"); SBAR();
;     ...
;     od = __builtin_amdgcn_mfma_f32_32x32x16_bf16(pa0, PK(l0, h0), od, 0, 0, 0);
;     od = __builtin_amdgcn_mfma_f32_32x32x16_bf16(pa1, PK(l1, h1), od, 0, 0, 0);
;     od = __builtin_amdgcn_mfma_f32_32x32x16_bf16(pa2, PK(l2, h2), od, 0, 0, 0);
;     od = __builtin_amdgcn_mfma_f32_32x32x16_bf16(pa3, PK(l3, h3), od, 0, 0, 0);
; template <int DK, bool PF, bool EARLY, bool PFD = false> ...
;     ...
;         const int vb = vb0 + cur * SHM_V;
;         pv_one<0>(o[0], vb, pa0, pa1, pa2, pa3); pv_one<1>(o[1], vb, pa0, pa1, pa2, pa3); pv_one<2>(o[2], vb, pa0, pa1, pa2, pa3); pv_one<3>(o[3], vb, pa0, pa1, pa2, pa3);
;         PSUB_AT(3);
;         if (j + 1 < ntile) SWRITE(cur ^ 1);
;         if (j + 3 < ntile) PREFETCH(j + 3);
;         __syncthreads();
	v_mfma_f32_32x32x16_bf16 v[2:17], v[82:85], v[246:249], v[2:17]
	ds_read_b64_tr_b16 v[98:99], v244 offset:0x200
	ds_read_b64_tr_b16 v[100:101], v244 offset:0xa00
	v_mfma_f32_32x32x16_bf16 v[2:17], v[86:89], v[250:253], v[2:17]
	ds_read_b64_tr_b16 v[102:103], v244 offset:0x1200
	ds_read_b64_tr_b16 v[104:105], v244 offset:0x1a00
	s_waitcnt lgkmcnt(6)
	v_mfma_f32_32x32x16_bf16 v[2:17], v[90:93], v[106:109], v[2:17]
	ds_read_b64_tr_b16 v[106:107], v244 offset:0x2200
	ds_read_b64_tr_b16 v[108:109], v244 offset:0x2a00
	ds_read_b64_tr_b16 v[240:241], v244 offset:0x3200
	ds_read_b64_tr_b16 v[242:243], v244 offset:0x3a00
	s_waitcnt lgkmcnt(8)
	v_mfma_f32_32x32x16_bf16 v[2:17], v[94:97], v[110:113], v[2:17]
	s_waitcnt lgkmcnt(6)
	v_mfma_f32_32x32x16_bf16 v[18:33], v[82:85], v[98:101], v[18:33]
	ds_read_b64_tr_b16 v[98:99], v244 offset:0x400
	ds_read_b64_tr_b16 v[100:101], v244 offset:0xc00
	s_waitcnt lgkmcnt(6)
	v_mfma_f32_32x32x16_bf16 v[18:33], v[86:89], v[102:105], v[18:33]
	ds_read_b64_tr_b16 v[102:103], v244 offset:0x1400
	ds_read_b64_tr_b16 v[104:105], v244 offset:0x1c00
	s_waitcnt lgkmcnt(6)
	v_mfma_f32_32x32x16_bf16 v[18:33], v[90:93], v[106:109], v[18:33]
	ds_read_b64_tr_b16 v[106:107], v244 offset:0x2400
	ds_read_b64_tr_b16 v[108:109], v244 offset:0x2c00
	ds_read_b64_tr_b16 v[110:111], v244 offset:0x3400
	ds_read_b64_tr_b16 v[112:113], v244 offset:0x3c00
	s_waitcnt lgkmcnt(8)
	v_mfma_f32_32x32x16_bf16 v[18:33], v[94:97], v[240:243], v[18:33]
	s_waitcnt lgkmcnt(6)
	v_mfma_f32_32x32x16_bf16 v[34:49], v[82:85], v[98:101], v[34:49]
	ds_read_b64_tr_b16 v[98:99], v244 offset:0x600
	ds_read_b64_tr_b16 v[100:101], v244 offset:0xe00
	s_waitcnt lgkmcnt(6)
	v_mfma_f32_32x32x16_bf16 v[34:49], v[86:89], v[102:105], v[34:49]
	ds_read_b64_tr_b16 v[102:103], v244 offset:0x1600
	ds_read_b64_tr_b16 v[104:105], v244 offset:0x1e00
	s_waitcnt lgkmcnt(6)
	v_mfma_f32_32x32x16_bf16 v[34:49], v[90:93], v[106:109], v[34:49]
	ds_read_b64_tr_b16 v[106:107], v244 offset:0x2600
	ds_read_b64_tr_b16 v[108:109], v244 offset:0x2e00
	ds_read_b64_tr_b16 v[240:241], v244 offset:0x3600
	ds_read_b64_tr_b16 v[242:243], v244 offset:0x3e00
	s_waitcnt lgkmcnt(8)
	v_mfma_f32_32x32x16_bf16 v[34:49], v[94:97], v[110:113], v[34:49]
	s_waitcnt lgkmcnt(6)
	v_mfma_f32_32x32x16_bf16 v[50:65], v[82:85], v[98:101], v[50:65]
	s_waitcnt lgkmcnt(0)
	s_xor_b32 s23, s23, 1
	s_mulk_i32 s23, 0x6000
	s_add_i32 s23, s23, 0
	v_add_u32_e32 v82, s23, v187
	s_waitcnt vmcnt(4)
	ds_write_b128 v82, v[166:169] offset:32768
	v_add_u32_e32 v82, s23, v193
	s_waitcnt vmcnt(3)
	ds_write_b128 v82, v[162:165] offset:32768
	v_mfma_f32_32x32x16_bf16 v[50:65], v[86:89], v[102:105], v[50:65]
	v_add_u32_e32 v82, s23, v197
	s_xor_b32 s23, s24, 0x4000
	s_add_i32 s20, s20, 0x18000
	s_add_i32 s21, s21, 0x10000
	v_add_u32_e32 v83, s23, v205
	s_cmp_eq_u32 s20, 0x660000
	s_waitcnt vmcnt(2)
	ds_write_b128 v82, v[178:181] offset:32768
	v_mfma_f32_32x32x16_bf16 v[50:65], v[90:93], v[106:109], v[50:65]
	s_waitcnt vmcnt(1)
	ds_write_b128 v83, v[170:173]
	s_waitcnt vmcnt(0)
	ds_write_b128 v83, v[174:177] offset:8192
	s_waitcnt lgkmcnt(0)
	s_barrier
	v_mfma_f32_32x32x16_bf16 v[50:65], v[94:97], v[240:243], v[50:65]
	s_cbranch_scc0 .LBB0_1200
	ds_read_b128 v[98:101], v217 offset:57344
	ds_read_b128 v[102:105], v218 offset:12288
	s_waitcnt lgkmcnt(1)
	v_mfma_f32_32x32x16_bf16 v[82:97], v[98:101], v[158:161], v[66:81]
	ds_read_b128 v[98:101], v219 offset:57344
	s_waitcnt lgkmcnt(1)
	v_mfma_f32_32x32x16_bf16 v[66:81], v[102:105], v[158:161], v[66:81]
	s_waitcnt lgkmcnt(0)
	v_mfma_f32_32x32x16_bf16 v[82:97], v[98:101], v[154:157], v[82:97]
	ds_read_b128 v[98:101], v220 offset:12288
	s_waitcnt lgkmcnt(0)
	v_mfma_f32_32x32x16_bf16 v[66:81], v[98:101], v[154:157], v[66:81]
	ds_read_b128 v[98:101], v221 offset:57344
	s_waitcnt lgkmcnt(0)
	v_mfma_f32_32x32x16_bf16 v[82:97], v[98:101], v[150:153], v[82:97]
	ds_read_b128 v[98:101], v222 offset:12288
	s_waitcnt lgkmcnt(0)
	v_mfma_f32_32x32x16_bf16 v[66:81], v[98:101], v[150:153], v[66:81]
	ds_read_b128 v[98:101], v223 offset:57344
	s_waitcnt lgkmcnt(0)
	v_mfma_f32_32x32x16_bf16 v[82:97], v[98:101], v[146:149], v[82:97]
	ds_read_b128 v[98:101], v224 offset:12288
	s_waitcnt lgkmcnt(0)
	v_mfma_f32_32x32x16_bf16 v[66:81], v[98:101], v[146:149], v[66:81]
	ds_read_b128 v[98:101], v217 offset:57472
	ds_read_b128 v[102:105], v218 offset:12416
	s_waitcnt lgkmcnt(1)
	v_mfma_f32_32x32x16_bf16 v[82:97], v[98:101], v[142:145], v[82:97]
	ds_read_b128 v[98:101], v219 offset:57472
	s_waitcnt lgkmcnt(1)
	v_mfma_f32_32x32x16_bf16 v[66:81], v[102:105], v[142:145], v[66:81]
	s_waitcnt lgkmcnt(0)
	v_mfma_f32_32x32x16_bf16 v[82:97], v[98:101], v[138:141], v[82:97]
	ds_read_b128 v[98:101], v220 offset:12416
	s_waitcnt lgkmcnt(0)
	v_mfma_f32_32x32x16_bf16 v[66:81], v[98:101], v[138:141], v[66:81]
	ds_read_b128 v[98:101], v221 offset:57472
	s_waitcnt lgkmcnt(0)
	v_mfma_f32_32x32x16_bf16 v[82:97], v[98:101], v[134:137], v[82:97]
	ds_read_b128 v[98:101], v222 offset:12416
	s_waitcnt lgkmcnt(0)
	v_mfma_f32_32x32x16_bf16 v[66:81], v[98:101], v[134:137], v[66:81]
	ds_read_b128 v[98:101], v223 offset:57472
	s_waitcnt lgkmcnt(0)
	v_mfma_f32_32x32x16_bf16 v[82:97], v[98:101], v[130:133], v[82:97]
	ds_read_b128 v[98:101], v224 offset:12416
	s_waitcnt lgkmcnt(0)
	v_mfma_f32_32x32x16_bf16 v[66:81], v[98:101], v[130:133], v[66:81]
	ds_read_b128 v[98:101], v217 offset:57600
	ds_read_b128 v[102:105], v218 offset:12544
	s_waitcnt lgkmcnt(1)
	v_mfma_f32_32x32x16_bf16 v[82:97], v[98:101], v[126:129], v[82:97]
	ds_read_b128 v[98:101], v219 offset:57600
	s_waitcnt lgkmcnt(1)
	v_mfma_f32_32x32x16_bf16 v[66:81], v[102:105], v[126:129], v[66:81]
	s_waitcnt lgkmcnt(0)
; #define PSUB_AT(k) do { if (PROBE_SUB == (k) && DK == PROBE_SUBDK) sacc = __builtin_amdgcn_readfirstlane(sacc + ((unsigned)__builtin_readcyclecounter() - ps_t0_)); } while (0)
; #define SBAR() __builtin_amdgcn_sched_barrier(0)
; template <int DK, bool PF, bool EARLY, bool PFD = false> ...
;     ...
;         const char* Kb = K_lds + cur * SHM_K;
; #pragma unroll
;         for (int d0 = 0; d0 < NQ; ++d0) {
;             const bf16x8 b0 = *reinterpret_cast<const bf16x8*>(Kb + kra_(d0 & 3) + (d0 >> 2) * 128);
;             const bf16x8 b1 = *reinterpret_cast<const bf16x8*>(Kb + kra_(d0 & 3) + (d0 >> 2) * 128 + 32 * DK * 2);
;             p0 = __builtin_amdgcn_mfma_f32_32x32x16_bf16(b0, qr[d0], p0, 0, 0, 0);
;             p1 = __builtin_amdgcn_mfma_f32_32x32x16_bf16(b1, qr[d0], p1, 0, 0, 0);
;             if ((d0 & 3) == 3) SBAR();
;         }
;         PSUB_AT(1);
;         if (!EARLY && j + 1 < ntile) SLOAD((j + 1) * 64);
;         float ps = 0.f, ps1 = 0.f;
; #pragma unroll
;         for (int r = 0; r < 16; ++r) { p0[r] = __builtin_amdgcn_exp2f(p0[r]); p1[r] = __builtin_amdgcn_exp2f(p1[r]); ps += p0[r]; asm("" : "+v"(ps)); ps1 += p1[r]; asm("" : "+v"(ps1)); }
;         l_reg += ps + ps1;
;         bf16x8 pa0, pa1, pa2, pa3;
;     ...
;         PK4(p0, 0, pa0); PK4(p0, 8, pa1); PK4(p1, 0, pa2); PK4(p1, 8, pa3);
;     ...
;         PSUB_AT(2);
;         const int vb = vb0 + cur * SHM_V;
;         pv_one<0>(o[0], vb, pa0, pa1, pa2, pa3); pv_one<1>(o[1], vb, pa0, pa1, pa2, pa3); pv_one<2>(o[2], vb, pa0, pa1, pa2, pa3); pv_one<3>(o[3], vb, pa0, pa1, pa2, pa3);
;         PSUB_AT(3);
;         if (j + 1 < ntile) SWRITE(cur ^ 1);
;         if (j + 3 < ntile) PREFETCH(j + 3);
;         __syncthreads();
;         PSUB_AT(4);
;     }
;     __builtin_amdgcn_s_setprio(0);
;     if (PF && !PFD) asm volatile("s_waitcnt vmcnt(0)" : "+v"(pf_dummy) :: "memory");
;     ...
; }
; __device__ __forceinline__ void row_recip(float l_reg, float* li_l  , int r32, int hi, float (&rli)[16]) {
;     { auto rr = __builtin_amdgcn_permlane32_swap(__float_as_uint(l_reg), __float_as_uint(l_reg), false, false); l_reg = __uint_as_float(rr[0]) + __uint_as_float(rr[1]); }
;     if (hi == 0) li_l[r32] = l_reg;
	v_mfma_f32_32x32x16_bf16 v[82:97], v[98:101], v[122:125], v[82:97]
	ds_read_b128 v[98:101], v220 offset:12544
	s_waitcnt lgkmcnt(0)
	v_mfma_f32_32x32x16_bf16 v[66:81], v[98:101], v[122:125], v[66:81]
	ds_read_b128 v[98:101], v221 offset:57600
	s_waitcnt lgkmcnt(0)
	v_mfma_f32_32x32x16_bf16 v[82:97], v[98:101], v[118:121], v[82:97]
	ds_read_b128 v[98:101], v222 offset:12544
	s_waitcnt lgkmcnt(0)
	v_mfma_f32_32x32x16_bf16 v[66:81], v[98:101], v[118:121], v[66:81]
	ds_read_b128 v[98:101], v223 offset:57600
	s_waitcnt lgkmcnt(0)
	v_mfma_f32_32x32x16_bf16 v[82:97], v[98:101], v[114:117], v[82:97]
	ds_read_b128 v[98:101], v224 offset:12544
	s_waitcnt lgkmcnt(0)
	v_mfma_f32_32x32x16_bf16 v[66:81], v[98:101], v[114:117], v[66:81]
	s_nop 11
	v_exp_f32_e32 v98, v66
	v_exp_f32_e32 v82, v82
	v_exp_f32_e32 v67, v67
	v_exp_f32_e32 v83, v83
	v_add_f32_e32 v99, 0, v98
	v_exp_f32_e32 v100, v68
	v_add_f32_e32 v66, 0, v82
	v_exp_f32_e32 v84, v84
	v_add_f32_e32 v99, v67, v99
	v_exp_f32_e32 v85, v85
	v_add_f32_e32 v66, v83, v66
	v_add_f32_e32 v68, v100, v99
	v_exp_f32_e32 v99, v69
	v_exp_f32_e32 v86, v86
	v_add_f32_e32 v66, v84, v66
	v_exp_f32_e32 v101, v70
	v_exp_f32_e32 v70, v87
	v_add_f32_e32 v66, v85, v66
	v_add_f32_e32 v68, v99, v68
	v_exp_f32_e32 v87, v71
	v_exp_f32_e32 v71, v88
	v_add_f32_e32 v66, v86, v66
	v_add_f32_e32 v68, v101, v68
	v_exp_f32_e32 v88, v72
	v_exp_f32_e32 v72, v89
	v_add_f32_e32 v66, v70, v66
	v_add_f32_e32 v68, v87, v68
	v_exp_f32_e32 v89, v73
	v_exp_f32_e32 v73, v90
	v_add_f32_e32 v66, v71, v66
	v_add_f32_e32 v68, v88, v68
	v_exp_f32_e32 v90, v74
	v_exp_f32_e32 v74, v91
	v_add_f32_e32 v66, v72, v66
	v_add_f32_e32 v68, v89, v68
	v_exp_f32_e32 v91, v75
	v_exp_f32_e32 v75, v92
	v_add_f32_e32 v66, v73, v66
	v_add_f32_e32 v68, v90, v68
	v_exp_f32_e32 v92, v76
	v_exp_f32_e32 v76, v93
	v_add_f32_e32 v66, v74, v66
	v_add_f32_e32 v68, v91, v68
	v_exp_f32_e32 v93, v77
	v_exp_f32_e32 v77, v94
	v_add_f32_e32 v66, v75, v66
	v_add_f32_e32 v68, v92, v68
	v_exp_f32_e32 v94, v78
	v_exp_f32_e32 v78, v95
	v_add_f32_e32 v66, v76, v66
	v_add_f32_e32 v68, v93, v68
	v_exp_f32_e32 v95, v79
	v_exp_f32_e32 v79, v96
	v_add_f32_e32 v66, v77, v66
	v_add_f32_e32 v68, v94, v68
	v_exp_f32_e32 v96, v80
	v_exp_f32_e32 v80, v97
	v_add_f32_e32 v66, v78, v66
	v_add_f32_e32 v68, v95, v68
	v_exp_f32_e32 v97, v81
	s_nop 0
	v_add_f32_e32 v66, v79, v66
	v_add_f32_e32 v68, v96, v68
	s_nop 0
	v_add_f32_e32 v66, v80, v66
	v_add_f32_e32 v68, v97, v68
	s_nop 0
	v_add_f32_e32 v66, v66, v68
	v_cvt_pk_bf16_f32 v68, v82, v83
	v_cvt_pk_bf16_f32 v69, v84, v85
	v_cvt_pk_bf16_f32 v70, v86, v70
	v_cvt_pk_bf16_f32 v71, v71, v72
	v_cvt_pk_bf16_f32 v72, v73, v74
	v_cvt_pk_bf16_f32 v73, v75, v76
	v_cvt_pk_bf16_f32 v74, v77, v78
	v_cvt_pk_bf16_f32 v75, v79, v80
	v_cvt_pk_bf16_f32 v76, v98, v67
	v_cvt_pk_bf16_f32 v77, v100, v99
	v_cvt_pk_bf16_f32 v78, v101, v87
	v_cvt_pk_bf16_f32 v79, v88, v89
	v_cvt_pk_bf16_f32 v80, v90, v91
	v_cvt_pk_bf16_f32 v81, v92, v93
	v_cvt_pk_bf16_f32 v82, v94, v95
	v_cvt_pk_bf16_f32 v83, v96, v97
	ds_read_b64_tr_b16 v[84:85], v225 offset:0
	ds_read_b64_tr_b16 v[86:87], v225 offset:0x800
	ds_read_b64_tr_b16 v[88:89], v225 offset:0x1000
	ds_read_b64_tr_b16 v[90:91], v225 offset:0x1800
	ds_read_b64_tr_b16 v[92:93], v225 offset:0x2000
	ds_read_b64_tr_b16 v[94:95], v225 offset:0x2800
	ds_read_b64_tr_b16 v[96:97], v225 offset:0x3000
	ds_read_b64_tr_b16 v[98:99], v225 offset:0x3800
	s_waitcnt lgkmcnt(0)
	v_add_f32_e32 v66, v188, v66
	v_permlane32_swap_b32_e32 v68, v70
	v_permlane32_swap_b32_e32 v69, v71
	v_permlane32_swap_b32_e32 v72, v74
	v_permlane32_swap_b32_e32 v73, v75
	v_permlane32_swap_b32_e32 v76, v78
	v_permlane32_swap_b32_e32 v77, v79
	v_permlane32_swap_b32_e32 v80, v82
	v_permlane32_swap_b32_e32 v81, v83
	v_mfma_f32_32x32x16_bf16 v[2:17], v[68:71], v[84:87], v[2:17]
	ds_read_b64_tr_b16 v[84:85], v225 offset:0x200
	ds_read_b64_tr_b16 v[86:87], v225 offset:0xa00
	v_mfma_f32_32x32x16_bf16 v[2:17], v[72:75], v[88:91], v[2:17]
	ds_read_b64_tr_b16 v[88:89], v225 offset:0x1200
	ds_read_b64_tr_b16 v[90:91], v225 offset:0x1a00
	v_mfma_f32_32x32x16_bf16 v[2:17], v[76:79], v[92:95], v[2:17]
	ds_read_b64_tr_b16 v[92:93], v225 offset:0x2200
	ds_read_b64_tr_b16 v[94:95], v225 offset:0x2a00
	ds_read_b64_tr_b16 v[100:101], v225 offset:0x3200
	ds_read_b64_tr_b16 v[102:103], v225 offset:0x3a00
	s_waitcnt lgkmcnt(0)
	v_mfma_f32_32x32x16_bf16 v[2:17], v[80:83], v[96:99], v[2:17]
	v_mfma_f32_32x32x16_bf16 v[18:33], v[68:71], v[84:87], v[18:33]
	ds_read_b64_tr_b16 v[84:85], v225 offset:0x400
	ds_read_b64_tr_b16 v[86:87], v225 offset:0xc00
	v_mfma_f32_32x32x16_bf16 v[18:33], v[72:75], v[88:91], v[18:33]
	ds_read_b64_tr_b16 v[88:89], v225 offset:0x1400
	ds_read_b64_tr_b16 v[90:91], v225 offset:0x1c00
	v_mfma_f32_32x32x16_bf16 v[18:33], v[76:79], v[92:95], v[18:33]
	ds_read_b64_tr_b16 v[92:93], v225 offset:0x2400
	ds_read_b64_tr_b16 v[94:95], v225 offset:0x2c00
	ds_read_b64_tr_b16 v[96:97], v225 offset:0x3400
	ds_read_b64_tr_b16 v[98:99], v225 offset:0x3c00
	s_waitcnt lgkmcnt(0)
	v_mfma_f32_32x32x16_bf16 v[18:33], v[80:83], v[100:103], v[18:33]
	v_mfma_f32_32x32x16_bf16 v[34:49], v[68:71], v[84:87], v[34:49]
	ds_read_b64_tr_b16 v[84:85], v225 offset:0x600
	ds_read_b64_tr_b16 v[86:87], v225 offset:0xe00
	v_mfma_f32_32x32x16_bf16 v[34:49], v[72:75], v[88:91], v[34:49]
	ds_read_b64_tr_b16 v[88:89], v225 offset:0x1600
	ds_read_b64_tr_b16 v[90:91], v225 offset:0x1e00
	v_mfma_f32_32x32x16_bf16 v[34:49], v[76:79], v[92:95], v[34:49]
	ds_read_b64_tr_b16 v[92:93], v225 offset:0x2600
	ds_read_b64_tr_b16 v[94:95], v225 offset:0x2e00
	ds_read_b64_tr_b16 v[100:101], v225 offset:0x3600
	ds_read_b64_tr_b16 v[102:103], v225 offset:0x3e00
	s_waitcnt lgkmcnt(0)
	v_mfma_f32_32x32x16_bf16 v[34:49], v[80:83], v[96:99], v[34:49]
	v_mfma_f32_32x32x16_bf16 v[50:65], v[68:71], v[84:87], v[50:65]
	s_barrier
	v_mfma_f32_32x32x16_bf16 v[50:65], v[72:75], v[88:91], v[50:65]
	v_mfma_f32_32x32x16_bf16 v[50:65], v[76:79], v[92:95], v[50:65]
	v_mfma_f32_32x32x16_bf16 v[50:65], v[80:83], v[100:103], v[50:65]
	s_setprio 0
	v_mov_b32_e32 v67, v66
	s_nop 1
	v_permlane32_swap_b32_e32 v66, v67
	s_and_saveexec_b64 s[8:9], s[6:7]
	s_cbranch_execz .LBB0_1186
	v_add_f32_e32 v66, v66, v67
	ds_write_b32 v227, v66
	s_branch .LBB0_1186
